# code placement (doc 9.3): v116's MLA up-projection epilogue rewrite with the downstream code padded back to the byte phase (mod 64) it had in v108
# speedup vs baseline: 1.0086x; 1.0086x over previous
; __device__ __forceinline__ KA kargs() { KA p = (KA)__builtin_amdgcn_kernarg_segment_ptr(); asm volatile("" : "+s"(p)); return p; }
; __device__ __forceinline__ void claim_fire(unsigned* ctr, int tid, int* pend) { if (tid == 0) *pend = (int)__hip_atomic_fetch_add(ctr, 1u, __ATOMIC_RELAXED, __HIP_MEMORY_SCOPE_AGENT); }
;     const Frame F = make_frame(lds, wv); const KA a = kargs();
;     const int* pos = (const int*)a->in[1];
;     unsigned* q0ctr = F.ctl + CW_QUEUE + ((l + qlo) * 8 + 0 + qs) * 64; unsigned* q1ctr = F.ctl + CW_QUEUE + ((l + qlo) * 8 + 1 + qs) * 64;
;     const bf16_t* QA = (const bf16_t*)(F.ws + WS_QA); const bf16_t* KAp = (const bf16_t*)(F.ws + WS_KA); const bf16_t* VAp = (const bf16_t*)(F.ws + WS_VA);
;     bf16_t* O = (bf16_t*)(F.ws + WS_O);
;     int pend = 0, lastm = 1 << 20;
;     at::claim_fire(q0ctr, F.tid, &pend);
; __global__ void __launch_bounds__(NTHR, 2) mk_fwd(Args args) {
;     ...
;         if (RUN(PH_ATTN1)) phase_attn1(lds, wv, l);
.LBB0_797:
	s_nop 0
	s_nop 0
	s_nop 0
	s_nop 0
	s_nop 0
	s_nop 0
	s_nop 0
	s_nop 0
	s_nop 0
	s_nop 0
	s_nop 0
	s_nop 0
	s_nop 0
	v_readlane_b32 s1, v255, 2
	v_readlane_b32 s40, v254, 62
	s_or_b32 s1, s1, 3
	v_readlane_b32 s41, v254, 63
	s_cmp_lt_i32 s1, s41
	s_cselect_b64 s[10:11], -1, 0
	s_and_b64 s[2:3], s[6:7], s[10:11]
	s_andn2_b64 vcc, exec, s[2:3]
	v_readlane_b32 s42, v255, 0
	v_readlane_b32 s43, v255, 1
	s_cbranch_vccnz .LBB0_853
	v_readlane_b32 s2, v253, 9
	v_readlane_b32 s3, v253, 10
	s_andn2_b64 vcc, exec, s[2:3]
	s_mov_b64 s[14:15], 0
	s_cbranch_vccnz .LBB0_800
	s_mov_b32 s2, -1
	s_waitcnt lgkmcnt(0)
	v_mbcnt_lo_u32_b32 v0, s2, 0
	v_mbcnt_hi_u32_b32 v0, s2, v0
	v_cmp_eq_u32_e32 vcc, 0, v0
	s_and_b64 s[14:15], vcc, exec
